# bf16 K-loops (G1,G2): LDS-DMA pieces addressed as SGPR base + 32-bit lane offset, no 64-bit VALU adds in load segments
# baseline (speedup 1.0000x reference)
.LBB0_310:
	v_add_u32_e32 v64, s34, v185
	ds_read_b128 v[130:133], v64
	ds_read_b128 v[134:137], v64 offset:1024
	ds_read_b128 v[138:141], v64 offset:2048
	ds_read_b128 v[142:145], v64 offset:3072
	v_add_u32_e32 v64, s37, v185
	ds_read_b128 v[158:161], v64
	ds_read_b128 v[162:165], v64 offset:1024
	ds_read_b128 v[166:169], v64 offset:2048
	ds_read_b128 v[170:173], v64 offset:3072
	s_add_u32 s26, s24, 0xfffc0080
	s_addc_u32 s27, s25, -1
	s_cmp_eq_u32 s56, 12
	s_cselect_b32 s29, s19, s27
	s_cselect_b32 s28, s33, s26
	s_cselect_b32 s27, s17, s55
	s_cselect_b32 s26, s53, s54
	s_add_i32 m0, s40, 0xc000
	ds_read_b128 v[174:177], v188
	ds_read_b128 v[178:181], v188 offset:1024
	ds_read_b128 v[190:193], v188 offset:2048
	ds_read_b128 v[212:215], v188 offset:3072
	ds_read_b128 v[216:219], v188 offset:4096
	ds_read_b128 v[220:223], v188 offset:5120
	ds_read_b128 v[224:227], v188 offset:6144
	ds_read_b128 v[228:231], v188 offset:7168
	global_load_lds_dwordx4 v154, s[24:25]
	s_add_i32 m0, s40, 0xe000
	s_nop 0
	global_load_lds_dwordx4 v156, s[24:25]
	s_waitcnt vmcnt(8)
	s_waitcnt lgkmcnt(0)
	s_barrier
	s_setprio 1
	s_waitcnt lgkmcnt(0)
	v_mfma_f32_16x16x32_bf16 v[126:129], v[130:133], v[174:177], v[126:129]
	v_mfma_f32_16x16x32_bf16 v[122:125], v[138:141], v[174:177], v[122:125]
	v_mfma_f32_16x16x32_bf16 v[118:121], v[130:133], v[190:193], v[118:121]
	v_mfma_f32_16x16x32_bf16 v[110:113], v[138:141], v[190:193], v[110:113]
	v_mfma_f32_16x16x32_bf16 v[102:105], v[130:133], v[216:219], v[102:105]
	v_mfma_f32_16x16x32_bf16 v[94:97], v[138:141], v[216:219], v[94:97]
	v_mfma_f32_16x16x32_bf16 v[86:89], v[130:133], v[224:227], v[86:89]
	v_mfma_f32_16x16x32_bf16 v[78:81], v[138:141], v[224:227], v[78:81]
	v_mfma_f32_16x16x32_bf16 v[126:129], v[134:137], v[178:181], v[126:129]
	v_mfma_f32_16x16x32_bf16 v[122:125], v[142:145], v[178:181], v[122:125]
	v_mfma_f32_16x16x32_bf16 v[118:121], v[134:137], v[212:215], v[118:121]
	v_mfma_f32_16x16x32_bf16 v[110:113], v[142:145], v[212:215], v[110:113]
	v_mfma_f32_16x16x32_bf16 v[102:105], v[134:137], v[220:223], v[102:105]
	v_mfma_f32_16x16x32_bf16 v[94:97], v[142:145], v[220:223], v[94:97]
	v_mfma_f32_16x16x32_bf16 v[86:89], v[134:137], v[228:231], v[86:89]
	v_mfma_f32_16x16x32_bf16 v[78:81], v[142:145], v[228:231], v[78:81]
	s_setprio 0
	s_setprio 1
	v_mfma_f32_16x16x32_bf16 v[114:117], v[158:161], v[174:177], v[114:117]
	v_mfma_f32_16x16x32_bf16 v[106:109], v[166:169], v[174:177], v[106:109]
	v_mfma_f32_16x16x32_bf16 v[98:101], v[158:161], v[190:193], v[98:101]
	v_mfma_f32_16x16x32_bf16 v[90:93], v[166:169], v[190:193], v[90:93]
	v_mfma_f32_16x16x32_bf16 v[82:85], v[158:161], v[216:219], v[82:85]
	v_mfma_f32_16x16x32_bf16 v[74:77], v[166:169], v[216:219], v[74:77]
	v_mfma_f32_16x16x32_bf16 v[70:73], v[158:161], v[224:227], v[70:73]
	v_mfma_f32_16x16x32_bf16 v[66:69], v[166:169], v[224:227], v[66:69]
	v_mfma_f32_16x16x32_bf16 v[114:117], v[162:165], v[178:181], v[114:117]
	v_mfma_f32_16x16x32_bf16 v[106:109], v[170:173], v[178:181], v[106:109]
	v_mfma_f32_16x16x32_bf16 v[98:101], v[162:165], v[212:215], v[98:101]
	v_mfma_f32_16x16x32_bf16 v[90:93], v[170:173], v[212:215], v[90:93]
	v_mfma_f32_16x16x32_bf16 v[82:85], v[162:165], v[220:223], v[82:85]
	v_mfma_f32_16x16x32_bf16 v[74:77], v[170:173], v[220:223], v[74:77]
	v_mfma_f32_16x16x32_bf16 v[70:73], v[162:165], v[228:231], v[70:73]
	v_mfma_f32_16x16x32_bf16 v[66:69], v[170:173], v[228:231], v[66:69]
	s_setprio 0
	s_barrier
	s_mov_b32 m0, s35
	s_add_u32 s58, s26, 0x40000
	ds_read_b128 v[174:177], v188 offset:16384
	ds_read_b128 v[178:181], v188 offset:17408
	ds_read_b128 v[190:193], v188 offset:18432
	ds_read_b128 v[212:215], v188 offset:19456
	ds_read_b128 v[216:219], v188 offset:20480
	ds_read_b128 v[220:223], v188 offset:21504
	ds_read_b128 v[224:227], v188 offset:22528
	ds_read_b128 v[228:231], v188 offset:23552
	global_load_lds_dwordx4 v150, s[26:27]
	s_mov_b32 m0, s36
	s_addc_u32 s59, s27, 0
	global_load_lds_dwordx4 v146, s[26:27]
	s_mov_b32 m0, s38
	s_nop 0
	global_load_lds_dwordx4 v150, s[58:59]
	s_mov_b32 m0, s39
	s_nop 0
	global_load_lds_dwordx4 v146, s[58:59]
	s_mov_b32 m0, s40
	s_nop 0
	global_load_lds_dwordx4 v152, s[28:29]
	s_mov_b32 m0, s41
	s_nop 0
	global_load_lds_dwordx4 v148, s[28:29]
	s_waitcnt vmcnt(8)
	s_waitcnt lgkmcnt(0)
	s_barrier
	s_setprio 1
	s_waitcnt lgkmcnt(0)
	v_mfma_f32_16x16x32_bf16 v[60:63], v[130:133], v[174:177], v[60:63]
	v_mfma_f32_16x16x32_bf16 v[56:59], v[138:141], v[174:177], v[56:59]
	v_mfma_f32_16x16x32_bf16 v[52:55], v[130:133], v[190:193], v[52:55]
	v_mfma_f32_16x16x32_bf16 v[44:47], v[138:141], v[190:193], v[44:47]
	v_mfma_f32_16x16x32_bf16 v[36:39], v[130:133], v[216:219], v[36:39]
	v_mfma_f32_16x16x32_bf16 v[28:31], v[138:141], v[216:219], v[28:31]
	v_mfma_f32_16x16x32_bf16 v[20:23], v[130:133], v[224:227], v[20:23]
	v_mfma_f32_16x16x32_bf16 v[12:15], v[138:141], v[224:227], v[12:15]
	v_mfma_f32_16x16x32_bf16 v[60:63], v[134:137], v[178:181], v[60:63]
	v_mfma_f32_16x16x32_bf16 v[56:59], v[142:145], v[178:181], v[56:59]
	v_mfma_f32_16x16x32_bf16 v[52:55], v[134:137], v[212:215], v[52:55]
	v_mfma_f32_16x16x32_bf16 v[44:47], v[142:145], v[212:215], v[44:47]
	v_mfma_f32_16x16x32_bf16 v[36:39], v[134:137], v[220:223], v[36:39]
	v_mfma_f32_16x16x32_bf16 v[28:31], v[142:145], v[220:223], v[28:31]
	v_mfma_f32_16x16x32_bf16 v[20:23], v[134:137], v[228:231], v[20:23]
	v_mfma_f32_16x16x32_bf16 v[12:15], v[142:145], v[228:231], v[12:15]
	s_setprio 0
	s_setprio 1
	v_mfma_f32_16x16x32_bf16 v[48:51], v[158:161], v[174:177], v[48:51]
	v_mfma_f32_16x16x32_bf16 v[40:43], v[166:169], v[174:177], v[40:43]
	v_mfma_f32_16x16x32_bf16 v[32:35], v[158:161], v[190:193], v[32:35]
	v_mfma_f32_16x16x32_bf16 v[24:27], v[166:169], v[190:193], v[24:27]
	v_mfma_f32_16x16x32_bf16 v[16:19], v[158:161], v[216:219], v[16:19]
	v_mfma_f32_16x16x32_bf16 v[8:11], v[166:169], v[216:219], v[8:11]
	v_mfma_f32_16x16x32_bf16 v[4:7], v[158:161], v[224:227], v[4:7]
	v_mfma_f32_16x16x32_bf16 v[0:3], v[166:169], v[224:227], v[0:3]
	v_mfma_f32_16x16x32_bf16 v[48:51], v[162:165], v[178:181], v[48:51]
	v_mfma_f32_16x16x32_bf16 v[40:43], v[170:173], v[178:181], v[40:43]
	v_mfma_f32_16x16x32_bf16 v[32:35], v[162:165], v[212:215], v[32:35]
	v_mfma_f32_16x16x32_bf16 v[24:27], v[170:173], v[212:215], v[24:27]
	v_mfma_f32_16x16x32_bf16 v[16:19], v[162:165], v[220:223], v[16:19]
	v_mfma_f32_16x16x32_bf16 v[8:11], v[170:173], v[220:223], v[8:11]
	v_mfma_f32_16x16x32_bf16 v[4:7], v[162:165], v[228:231], v[4:7]
	v_mfma_f32_16x16x32_bf16 v[0:3], v[170:173], v[228:231], v[0:3]
	s_setprio 0
	s_barrier
	v_add_u32_e32 v64, s44, v185
	ds_read_b128 v[130:133], v64
	ds_read_b128 v[134:137], v64 offset:1024
	ds_read_b128 v[138:141], v64 offset:2048
	ds_read_b128 v[142:145], v64 offset:3072
	v_add_u32_e32 v64, s49, v185
	ds_read_b128 v[158:161], v64
	ds_read_b128 v[162:165], v64 offset:1024
	ds_read_b128 v[166:169], v64 offset:2048
	ds_read_b128 v[170:173], v64 offset:3072
	s_add_u32 s28, s28, 0x40000
	s_addc_u32 s29, s29, 0
	s_mov_b32 m0, s42
	ds_read_b128 v[174:177], v188 offset:32768
	ds_read_b128 v[178:181], v188 offset:33792
	ds_read_b128 v[190:193], v188 offset:34816
	ds_read_b128 v[212:215], v188 offset:35840
	ds_read_b128 v[216:219], v188 offset:36864
	ds_read_b128 v[220:223], v188 offset:37888
	ds_read_b128 v[224:227], v188 offset:38912
	ds_read_b128 v[228:231], v188 offset:39936
	global_load_lds_dwordx4 v152, s[28:29]
	s_mov_b32 m0, s43
	s_nop 0
	global_load_lds_dwordx4 v148, s[28:29]
	s_waitcnt vmcnt(8)
	s_waitcnt lgkmcnt(0)
	s_barrier
	s_setprio 1
	s_waitcnt lgkmcnt(0)
	v_mfma_f32_16x16x32_bf16 v[126:129], v[130:133], v[174:177], v[126:129]
	v_mfma_f32_16x16x32_bf16 v[122:125], v[138:141], v[174:177], v[122:125]
	v_mfma_f32_16x16x32_bf16 v[118:121], v[130:133], v[190:193], v[118:121]
	v_mfma_f32_16x16x32_bf16 v[110:113], v[138:141], v[190:193], v[110:113]
	v_mfma_f32_16x16x32_bf16 v[102:105], v[130:133], v[216:219], v[102:105]
	v_mfma_f32_16x16x32_bf16 v[94:97], v[138:141], v[216:219], v[94:97]
	v_mfma_f32_16x16x32_bf16 v[86:89], v[130:133], v[224:227], v[86:89]
	v_mfma_f32_16x16x32_bf16 v[78:81], v[138:141], v[224:227], v[78:81]
	v_mfma_f32_16x16x32_bf16 v[126:129], v[134:137], v[178:181], v[126:129]
	v_mfma_f32_16x16x32_bf16 v[122:125], v[142:145], v[178:181], v[122:125]
	v_mfma_f32_16x16x32_bf16 v[118:121], v[134:137], v[212:215], v[118:121]
	v_mfma_f32_16x16x32_bf16 v[110:113], v[142:145], v[212:215], v[110:113]
	v_mfma_f32_16x16x32_bf16 v[102:105], v[134:137], v[220:223], v[102:105]
	v_mfma_f32_16x16x32_bf16 v[94:97], v[142:145], v[220:223], v[94:97]
	v_mfma_f32_16x16x32_bf16 v[86:89], v[134:137], v[228:231], v[86:89]
	v_mfma_f32_16x16x32_bf16 v[78:81], v[142:145], v[228:231], v[78:81]
	s_setprio 0
	s_setprio 1
	v_mfma_f32_16x16x32_bf16 v[114:117], v[158:161], v[174:177], v[114:117]
	v_mfma_f32_16x16x32_bf16 v[106:109], v[166:169], v[174:177], v[106:109]
	v_mfma_f32_16x16x32_bf16 v[98:101], v[158:161], v[190:193], v[98:101]
	v_mfma_f32_16x16x32_bf16 v[90:93], v[166:169], v[190:193], v[90:93]
	v_mfma_f32_16x16x32_bf16 v[82:85], v[158:161], v[216:219], v[82:85]
	v_mfma_f32_16x16x32_bf16 v[74:77], v[166:169], v[216:219], v[74:77]
	v_mfma_f32_16x16x32_bf16 v[70:73], v[158:161], v[224:227], v[70:73]
	v_mfma_f32_16x16x32_bf16 v[66:69], v[166:169], v[224:227], v[66:69]
	v_mfma_f32_16x16x32_bf16 v[114:117], v[162:165], v[178:181], v[114:117]
	v_mfma_f32_16x16x32_bf16 v[106:109], v[170:173], v[178:181], v[106:109]
	v_mfma_f32_16x16x32_bf16 v[98:101], v[162:165], v[212:215], v[98:101]
	v_mfma_f32_16x16x32_bf16 v[90:93], v[170:173], v[212:215], v[90:93]
	v_mfma_f32_16x16x32_bf16 v[82:85], v[162:165], v[220:223], v[82:85]
	v_mfma_f32_16x16x32_bf16 v[74:77], v[170:173], v[220:223], v[74:77]
	v_mfma_f32_16x16x32_bf16 v[70:73], v[162:165], v[228:231], v[70:73]
	v_mfma_f32_16x16x32_bf16 v[66:69], v[170:173], v[228:231], v[66:69]
	s_setprio 0
	s_barrier
	s_mov_b32 m0, s45
	s_add_u32 s100, s26, s68
	s_addc_u32 s101, s27, s69
	s_add_u32 s26, s26, 0x40080
	ds_read_b128 v[174:177], v188 offset:49152
	ds_read_b128 v[178:181], v188 offset:50176
	ds_read_b128 v[190:193], v188 offset:51200
	ds_read_b128 v[212:215], v188 offset:52224
	ds_read_b128 v[216:219], v188 offset:53248
	ds_read_b128 v[220:223], v188 offset:54272
	ds_read_b128 v[224:227], v188 offset:55296
	ds_read_b128 v[228:231], v188 offset:56320
	global_load_lds_dwordx4 v150, s[100:101]
	s_mov_b32 m0, s46
	s_addc_u32 s27, s27, 0
	global_load_lds_dwordx4 v146, s[100:101]
	s_mov_b32 m0, s50
	s_add_u32 s100, s28, s68
	global_load_lds_dwordx4 v150, s[26:27]
	s_addc_u32 s101, s29, s69
	s_mov_b32 m0, s51
	s_sub_u32 s100, s100, 0x40000
	global_load_lds_dwordx4 v146, s[26:27]
	s_subb_u32 s101, s101, 0
	s_mov_b32 m0, s47
	s_nop 0
	global_load_lds_dwordx4 v152, s[100:101]
	s_mov_b32 m0, s48
	s_nop 0
	global_load_lds_dwordx4 v148, s[100:101]
	s_waitcnt vmcnt(8)
	s_waitcnt lgkmcnt(0)
	s_barrier
	s_setprio 1
	s_waitcnt lgkmcnt(0)
	v_mfma_f32_16x16x32_bf16 v[60:63], v[130:133], v[174:177], v[60:63]
	v_mfma_f32_16x16x32_bf16 v[56:59], v[138:141], v[174:177], v[56:59]
	v_mfma_f32_16x16x32_bf16 v[52:55], v[130:133], v[190:193], v[52:55]
	v_mfma_f32_16x16x32_bf16 v[44:47], v[138:141], v[190:193], v[44:47]
	v_mfma_f32_16x16x32_bf16 v[36:39], v[130:133], v[216:219], v[36:39]
	v_mfma_f32_16x16x32_bf16 v[28:31], v[138:141], v[216:219], v[28:31]
	v_mfma_f32_16x16x32_bf16 v[20:23], v[130:133], v[224:227], v[20:23]
	v_mfma_f32_16x16x32_bf16 v[12:15], v[138:141], v[224:227], v[12:15]
	v_mfma_f32_16x16x32_bf16 v[60:63], v[134:137], v[178:181], v[60:63]
	v_mfma_f32_16x16x32_bf16 v[56:59], v[142:145], v[178:181], v[56:59]
	v_mfma_f32_16x16x32_bf16 v[52:55], v[134:137], v[212:215], v[52:55]
	v_mfma_f32_16x16x32_bf16 v[44:47], v[142:145], v[212:215], v[44:47]
	v_mfma_f32_16x16x32_bf16 v[36:39], v[134:137], v[220:223], v[36:39]
	v_mfma_f32_16x16x32_bf16 v[28:31], v[142:145], v[220:223], v[28:31]
	v_mfma_f32_16x16x32_bf16 v[20:23], v[134:137], v[228:231], v[20:23]
	v_mfma_f32_16x16x32_bf16 v[12:15], v[142:145], v[228:231], v[12:15]
	s_setprio 0
	s_setprio 1
	v_mfma_f32_16x16x32_bf16 v[48:51], v[158:161], v[174:177], v[48:51]
	v_mfma_f32_16x16x32_bf16 v[40:43], v[166:169], v[174:177], v[40:43]
	v_mfma_f32_16x16x32_bf16 v[32:35], v[158:161], v[190:193], v[32:35]
	v_mfma_f32_16x16x32_bf16 v[24:27], v[166:169], v[190:193], v[24:27]
	v_mfma_f32_16x16x32_bf16 v[16:19], v[158:161], v[216:219], v[16:19]
	v_mfma_f32_16x16x32_bf16 v[8:11], v[166:169], v[216:219], v[8:11]
	v_mfma_f32_16x16x32_bf16 v[4:7], v[158:161], v[224:227], v[4:7]
	v_mfma_f32_16x16x32_bf16 v[0:3], v[166:169], v[224:227], v[0:3]
	v_mfma_f32_16x16x32_bf16 v[48:51], v[162:165], v[178:181], v[48:51]
	v_mfma_f32_16x16x32_bf16 v[40:43], v[170:173], v[178:181], v[40:43]
	v_mfma_f32_16x16x32_bf16 v[32:35], v[162:165], v[212:215], v[32:35]
	v_mfma_f32_16x16x32_bf16 v[24:27], v[170:173], v[212:215], v[24:27]
	v_mfma_f32_16x16x32_bf16 v[16:19], v[162:165], v[220:223], v[16:19]
	v_mfma_f32_16x16x32_bf16 v[8:11], v[170:173], v[220:223], v[8:11]
	v_mfma_f32_16x16x32_bf16 v[4:7], v[162:165], v[228:231], v[4:7]
	v_mfma_f32_16x16x32_bf16 v[0:3], v[170:173], v[228:231], v[0:3]
	s_setprio 0
	s_barrier
	s_add_i32 s56, s56, 2
	s_add_u32 s24, s24, 0x100
	s_addc_u32 s25, s25, 0
	s_add_u32 s54, s54, 0x100
	s_addc_u32 s55, s55, 0
	s_cmp_gt_u32 s56, 13
	s_cbranch_scc0 .LBB0_310
	s_and_b64 vcc, exec, s[14:15]
	s_cbranch_vccz .LBB0_313
	s_barrier

.LBB0_814:
	v_add_u32_e32 v64, s11, v173
	ds_read_b128 v[66:69], v64
	ds_read_b128 v[70:73], v64 offset:1024
	ds_read_b128 v[74:77], v64 offset:2048
	ds_read_b128 v[78:81], v64 offset:3072
	v_add_u32_e32 v64, s34, v173
	ds_read_b128 v[146:149], v64
	ds_read_b128 v[150:153], v64 offset:1024
	ds_read_b128 v[166:169], v64 offset:2048
	ds_read_b128 v[176:179], v64 offset:3072
	s_add_u32 s4, s0, 0xfffc0080
	s_addc_u32 s5, s1, -1
	s_cmp_eq_u32 s61, 12
	s_cselect_b32 s27, s55, s5
	s_cselect_b32 s26, s56, s4
	s_cselect_b32 s5, s57, s60
	s_cselect_b32 s4, s58, s59
	s_add_i32 m0, s37, 0xc000
	ds_read_b128 v[180:183], v175
	ds_read_b128 v[184:187], v175 offset:1024
	ds_read_b128 v[188:191], v175 offset:2048
	ds_read_b128 v[192:195], v175 offset:3072
	ds_read_b128 v[212:215], v175 offset:4096
	ds_read_b128 v[216:219], v175 offset:5120
	ds_read_b128 v[220:223], v175 offset:6144
	ds_read_b128 v[224:227], v175 offset:7168
	global_load_lds_dwordx4 v162, s[0:1]
	s_add_i32 m0, s37, 0xe000
	s_nop 0
	global_load_lds_dwordx4 v164, s[0:1]
	s_waitcnt vmcnt(8)
	s_waitcnt lgkmcnt(0)
	s_barrier
	s_setprio 1
	s_waitcnt lgkmcnt(0)
	v_mfma_f32_16x16x32_bf16 v[142:145], v[66:69], v[180:183], v[142:145]
	v_mfma_f32_16x16x32_bf16 v[138:141], v[74:77], v[180:183], v[138:141]
	v_mfma_f32_16x16x32_bf16 v[126:129], v[66:69], v[188:191], v[126:129]
	v_mfma_f32_16x16x32_bf16 v[122:125], v[74:77], v[188:191], v[122:125]
	v_mfma_f32_16x16x32_bf16 v[110:113], v[66:69], v[212:215], v[110:113]
	v_mfma_f32_16x16x32_bf16 v[106:109], v[74:77], v[212:215], v[106:109]
	v_mfma_f32_16x16x32_bf16 v[94:97], v[66:69], v[220:223], v[94:97]
	v_mfma_f32_16x16x32_bf16 v[90:93], v[74:77], v[220:223], v[90:93]
	v_mfma_f32_16x16x32_bf16 v[142:145], v[70:73], v[184:187], v[142:145]
	v_mfma_f32_16x16x32_bf16 v[138:141], v[78:81], v[184:187], v[138:141]
	v_mfma_f32_16x16x32_bf16 v[126:129], v[70:73], v[192:195], v[126:129]
	v_mfma_f32_16x16x32_bf16 v[122:125], v[78:81], v[192:195], v[122:125]
	v_mfma_f32_16x16x32_bf16 v[110:113], v[70:73], v[216:219], v[110:113]
	v_mfma_f32_16x16x32_bf16 v[106:109], v[78:81], v[216:219], v[106:109]
	v_mfma_f32_16x16x32_bf16 v[94:97], v[70:73], v[224:227], v[94:97]
	v_mfma_f32_16x16x32_bf16 v[90:93], v[78:81], v[224:227], v[90:93]
	s_setprio 0
	s_setprio 1
	v_mfma_f32_16x16x32_bf16 v[134:137], v[146:149], v[180:183], v[134:137]
	v_mfma_f32_16x16x32_bf16 v[130:133], v[166:169], v[180:183], v[130:133]
	v_mfma_f32_16x16x32_bf16 v[118:121], v[146:149], v[188:191], v[118:121]
	v_mfma_f32_16x16x32_bf16 v[114:117], v[166:169], v[188:191], v[114:117]
	v_mfma_f32_16x16x32_bf16 v[102:105], v[146:149], v[212:215], v[102:105]
	v_mfma_f32_16x16x32_bf16 v[98:101], v[166:169], v[212:215], v[98:101]
	v_mfma_f32_16x16x32_bf16 v[86:89], v[146:149], v[220:223], v[86:89]
	v_mfma_f32_16x16x32_bf16 v[82:85], v[166:169], v[220:223], v[82:85]
	v_mfma_f32_16x16x32_bf16 v[134:137], v[150:153], v[184:187], v[134:137]
	v_mfma_f32_16x16x32_bf16 v[130:133], v[176:179], v[184:187], v[130:133]
	v_mfma_f32_16x16x32_bf16 v[118:121], v[150:153], v[192:195], v[118:121]
	v_mfma_f32_16x16x32_bf16 v[114:117], v[176:179], v[192:195], v[114:117]
	v_mfma_f32_16x16x32_bf16 v[102:105], v[150:153], v[216:219], v[102:105]
	v_mfma_f32_16x16x32_bf16 v[98:101], v[176:179], v[216:219], v[98:101]
	v_mfma_f32_16x16x32_bf16 v[86:89], v[150:153], v[224:227], v[86:89]
	v_mfma_f32_16x16x32_bf16 v[82:85], v[176:179], v[224:227], v[82:85]
	s_setprio 0
	s_barrier
	s_mov_b32 m0, s31
	s_add_u32 s62, s4, 0x40000
	ds_read_b128 v[180:183], v175 offset:16384
	ds_read_b128 v[184:187], v175 offset:17408
	ds_read_b128 v[188:191], v175 offset:18432
	ds_read_b128 v[192:195], v175 offset:19456
	ds_read_b128 v[212:215], v175 offset:20480
	ds_read_b128 v[216:219], v175 offset:21504
	ds_read_b128 v[220:223], v175 offset:22528
	ds_read_b128 v[224:227], v175 offset:23552
	global_load_lds_dwordx4 v158, s[4:5]
	s_mov_b32 m0, s33
	s_addc_u32 s63, s5, 0
	global_load_lds_dwordx4 v154, s[4:5]
	s_mov_b32 m0, s35
	s_nop 0
	global_load_lds_dwordx4 v158, s[62:63]
	s_mov_b32 m0, s36
	s_nop 0
	global_load_lds_dwordx4 v154, s[62:63]
	s_mov_b32 m0, s37
	s_nop 0
	global_load_lds_dwordx4 v160, s[26:27]
	s_mov_b32 m0, s38
	s_nop 0
	global_load_lds_dwordx4 v156, s[26:27]
	s_waitcnt vmcnt(8)
	s_waitcnt lgkmcnt(0)
	s_barrier
	s_setprio 1
	s_waitcnt lgkmcnt(0)
	v_mfma_f32_16x16x32_bf16 v[60:63], v[66:69], v[180:183], v[60:63]
	v_mfma_f32_16x16x32_bf16 v[56:59], v[74:77], v[180:183], v[56:59]
	v_mfma_f32_16x16x32_bf16 v[44:47], v[66:69], v[188:191], v[44:47]
	v_mfma_f32_16x16x32_bf16 v[40:43], v[74:77], v[188:191], v[40:43]
	v_mfma_f32_16x16x32_bf16 v[28:31], v[66:69], v[212:215], v[28:31]
	v_mfma_f32_16x16x32_bf16 v[24:27], v[74:77], v[212:215], v[24:27]
	v_mfma_f32_16x16x32_bf16 v[12:15], v[66:69], v[220:223], v[12:15]
	v_mfma_f32_16x16x32_bf16 v[8:11], v[74:77], v[220:223], v[8:11]
	v_mfma_f32_16x16x32_bf16 v[60:63], v[70:73], v[184:187], v[60:63]
	v_mfma_f32_16x16x32_bf16 v[56:59], v[78:81], v[184:187], v[56:59]
	v_mfma_f32_16x16x32_bf16 v[44:47], v[70:73], v[192:195], v[44:47]
	v_mfma_f32_16x16x32_bf16 v[40:43], v[78:81], v[192:195], v[40:43]
	v_mfma_f32_16x16x32_bf16 v[28:31], v[70:73], v[216:219], v[28:31]
	v_mfma_f32_16x16x32_bf16 v[24:27], v[78:81], v[216:219], v[24:27]
	v_mfma_f32_16x16x32_bf16 v[12:15], v[70:73], v[224:227], v[12:15]
	v_mfma_f32_16x16x32_bf16 v[8:11], v[78:81], v[224:227], v[8:11]
	s_setprio 0
	s_setprio 1
	v_mfma_f32_16x16x32_bf16 v[52:55], v[146:149], v[180:183], v[52:55]
	v_mfma_f32_16x16x32_bf16 v[48:51], v[166:169], v[180:183], v[48:51]
	v_mfma_f32_16x16x32_bf16 v[36:39], v[146:149], v[188:191], v[36:39]
	v_mfma_f32_16x16x32_bf16 v[32:35], v[166:169], v[188:191], v[32:35]
	v_mfma_f32_16x16x32_bf16 v[20:23], v[146:149], v[212:215], v[20:23]
	v_mfma_f32_16x16x32_bf16 v[16:19], v[166:169], v[212:215], v[16:19]
	v_mfma_f32_16x16x32_bf16 v[4:7], v[146:149], v[220:223], v[4:7]
	v_mfma_f32_16x16x32_bf16 v[0:3], v[166:169], v[220:223], v[0:3]
	v_mfma_f32_16x16x32_bf16 v[52:55], v[150:153], v[184:187], v[52:55]
	v_mfma_f32_16x16x32_bf16 v[48:51], v[176:179], v[184:187], v[48:51]
	v_mfma_f32_16x16x32_bf16 v[36:39], v[150:153], v[192:195], v[36:39]
	v_mfma_f32_16x16x32_bf16 v[32:35], v[176:179], v[192:195], v[32:35]
	v_mfma_f32_16x16x32_bf16 v[20:23], v[150:153], v[216:219], v[20:23]
	v_mfma_f32_16x16x32_bf16 v[16:19], v[176:179], v[216:219], v[16:19]
	v_mfma_f32_16x16x32_bf16 v[4:7], v[150:153], v[224:227], v[4:7]
	v_mfma_f32_16x16x32_bf16 v[0:3], v[176:179], v[224:227], v[0:3]
	s_setprio 0
	s_barrier
	v_add_u32_e32 v64, s43, v173
	ds_read_b128 v[66:69], v64
	ds_read_b128 v[70:73], v64 offset:1024
	ds_read_b128 v[74:77], v64 offset:2048
	ds_read_b128 v[78:81], v64 offset:3072
	v_add_u32_e32 v64, s48, v173
	ds_read_b128 v[146:149], v64
	ds_read_b128 v[150:153], v64 offset:1024
	ds_read_b128 v[166:169], v64 offset:2048
	ds_read_b128 v[176:179], v64 offset:3072
	s_add_u32 s26, s26, 0x40000
	s_addc_u32 s27, s27, 0
	s_mov_b32 m0, s39
	ds_read_b128 v[180:183], v175 offset:32768
	ds_read_b128 v[184:187], v175 offset:33792
	ds_read_b128 v[188:191], v175 offset:34816
	ds_read_b128 v[192:195], v175 offset:35840
	ds_read_b128 v[212:215], v175 offset:36864
	ds_read_b128 v[216:219], v175 offset:37888
	ds_read_b128 v[220:223], v175 offset:38912
	ds_read_b128 v[224:227], v175 offset:39936
	global_load_lds_dwordx4 v160, s[26:27]
	s_mov_b32 m0, s40
	s_nop 0
	global_load_lds_dwordx4 v156, s[26:27]
	s_waitcnt vmcnt(8)
	s_waitcnt lgkmcnt(0)
	s_barrier
	s_setprio 1
	s_waitcnt lgkmcnt(0)
	v_mfma_f32_16x16x32_bf16 v[142:145], v[66:69], v[180:183], v[142:145]
	v_mfma_f32_16x16x32_bf16 v[138:141], v[74:77], v[180:183], v[138:141]
	v_mfma_f32_16x16x32_bf16 v[126:129], v[66:69], v[188:191], v[126:129]
	v_mfma_f32_16x16x32_bf16 v[122:125], v[74:77], v[188:191], v[122:125]
	v_mfma_f32_16x16x32_bf16 v[110:113], v[66:69], v[212:215], v[110:113]
	v_mfma_f32_16x16x32_bf16 v[106:109], v[74:77], v[212:215], v[106:109]
	v_mfma_f32_16x16x32_bf16 v[94:97], v[66:69], v[220:223], v[94:97]
	v_mfma_f32_16x16x32_bf16 v[90:93], v[74:77], v[220:223], v[90:93]
	v_mfma_f32_16x16x32_bf16 v[142:145], v[70:73], v[184:187], v[142:145]
	v_mfma_f32_16x16x32_bf16 v[138:141], v[78:81], v[184:187], v[138:141]
	v_mfma_f32_16x16x32_bf16 v[126:129], v[70:73], v[192:195], v[126:129]
	v_mfma_f32_16x16x32_bf16 v[122:125], v[78:81], v[192:195], v[122:125]
	v_mfma_f32_16x16x32_bf16 v[110:113], v[70:73], v[216:219], v[110:113]
	v_mfma_f32_16x16x32_bf16 v[106:109], v[78:81], v[216:219], v[106:109]
	v_mfma_f32_16x16x32_bf16 v[94:97], v[70:73], v[224:227], v[94:97]
	v_mfma_f32_16x16x32_bf16 v[90:93], v[78:81], v[224:227], v[90:93]
	s_setprio 0
	s_setprio 1
	v_mfma_f32_16x16x32_bf16 v[134:137], v[146:149], v[180:183], v[134:137]
	v_mfma_f32_16x16x32_bf16 v[130:133], v[166:169], v[180:183], v[130:133]
	v_mfma_f32_16x16x32_bf16 v[118:121], v[146:149], v[188:191], v[118:121]
	v_mfma_f32_16x16x32_bf16 v[114:117], v[166:169], v[188:191], v[114:117]
	v_mfma_f32_16x16x32_bf16 v[102:105], v[146:149], v[212:215], v[102:105]
	v_mfma_f32_16x16x32_bf16 v[98:101], v[166:169], v[212:215], v[98:101]
	v_mfma_f32_16x16x32_bf16 v[86:89], v[146:149], v[220:223], v[86:89]
	v_mfma_f32_16x16x32_bf16 v[82:85], v[166:169], v[220:223], v[82:85]
	v_mfma_f32_16x16x32_bf16 v[134:137], v[150:153], v[184:187], v[134:137]
	v_mfma_f32_16x16x32_bf16 v[130:133], v[176:179], v[184:187], v[130:133]
	v_mfma_f32_16x16x32_bf16 v[118:121], v[150:153], v[192:195], v[118:121]
	v_mfma_f32_16x16x32_bf16 v[114:117], v[176:179], v[192:195], v[114:117]
	v_mfma_f32_16x16x32_bf16 v[102:105], v[150:153], v[216:219], v[102:105]
	v_mfma_f32_16x16x32_bf16 v[98:101], v[176:179], v[216:219], v[98:101]
	v_mfma_f32_16x16x32_bf16 v[86:89], v[150:153], v[224:227], v[86:89]
	v_mfma_f32_16x16x32_bf16 v[82:85], v[176:179], v[224:227], v[82:85]
	s_setprio 0
	s_barrier
	s_mov_b32 m0, s44
	s_add_u32 s100, s4, s68
	s_addc_u32 s101, s5, s69
	s_add_u32 s4, s4, 0x40080
	ds_read_b128 v[180:183], v175 offset:49152
	ds_read_b128 v[184:187], v175 offset:50176
	ds_read_b128 v[188:191], v175 offset:51200
	ds_read_b128 v[192:195], v175 offset:52224
	ds_read_b128 v[212:215], v175 offset:53248
	ds_read_b128 v[216:219], v175 offset:54272
	ds_read_b128 v[220:223], v175 offset:55296
	ds_read_b128 v[224:227], v175 offset:56320
	global_load_lds_dwordx4 v158, s[100:101]
	s_mov_b32 m0, s45
	s_addc_u32 s5, s5, 0
	global_load_lds_dwordx4 v154, s[100:101]
	s_mov_b32 m0, s49
	s_add_u32 s100, s26, s68
	global_load_lds_dwordx4 v158, s[4:5]
	s_addc_u32 s101, s27, s69
	s_mov_b32 m0, s50
	s_sub_u32 s100, s100, 0x40000
	global_load_lds_dwordx4 v154, s[4:5]
	s_subb_u32 s101, s101, 0
	s_mov_b32 m0, s46
	s_nop 0
	global_load_lds_dwordx4 v160, s[100:101]
	s_mov_b32 m0, s47
	s_nop 0
	global_load_lds_dwordx4 v156, s[100:101]
	s_waitcnt vmcnt(8)
	s_waitcnt lgkmcnt(0)
	s_barrier
	s_setprio 1
	s_waitcnt lgkmcnt(0)
	v_mfma_f32_16x16x32_bf16 v[60:63], v[66:69], v[180:183], v[60:63]
	v_mfma_f32_16x16x32_bf16 v[56:59], v[74:77], v[180:183], v[56:59]
	v_mfma_f32_16x16x32_bf16 v[44:47], v[66:69], v[188:191], v[44:47]
	v_mfma_f32_16x16x32_bf16 v[40:43], v[74:77], v[188:191], v[40:43]
	v_mfma_f32_16x16x32_bf16 v[28:31], v[66:69], v[212:215], v[28:31]
	v_mfma_f32_16x16x32_bf16 v[24:27], v[74:77], v[212:215], v[24:27]
	v_mfma_f32_16x16x32_bf16 v[12:15], v[66:69], v[220:223], v[12:15]
	v_mfma_f32_16x16x32_bf16 v[8:11], v[74:77], v[220:223], v[8:11]
	v_mfma_f32_16x16x32_bf16 v[60:63], v[70:73], v[184:187], v[60:63]
	v_mfma_f32_16x16x32_bf16 v[56:59], v[78:81], v[184:187], v[56:59]
	v_mfma_f32_16x16x32_bf16 v[44:47], v[70:73], v[192:195], v[44:47]
	v_mfma_f32_16x16x32_bf16 v[40:43], v[78:81], v[192:195], v[40:43]
	v_mfma_f32_16x16x32_bf16 v[28:31], v[70:73], v[216:219], v[28:31]
	v_mfma_f32_16x16x32_bf16 v[24:27], v[78:81], v[216:219], v[24:27]
	v_mfma_f32_16x16x32_bf16 v[12:15], v[70:73], v[224:227], v[12:15]
	v_mfma_f32_16x16x32_bf16 v[8:11], v[78:81], v[224:227], v[8:11]
	s_setprio 0
	s_setprio 1
	v_mfma_f32_16x16x32_bf16 v[52:55], v[146:149], v[180:183], v[52:55]
	v_mfma_f32_16x16x32_bf16 v[48:51], v[166:169], v[180:183], v[48:51]
	v_mfma_f32_16x16x32_bf16 v[36:39], v[146:149], v[188:191], v[36:39]
	v_mfma_f32_16x16x32_bf16 v[32:35], v[166:169], v[188:191], v[32:35]
	v_mfma_f32_16x16x32_bf16 v[20:23], v[146:149], v[212:215], v[20:23]
	v_mfma_f32_16x16x32_bf16 v[16:19], v[166:169], v[212:215], v[16:19]
	v_mfma_f32_16x16x32_bf16 v[4:7], v[146:149], v[220:223], v[4:7]
	v_mfma_f32_16x16x32_bf16 v[0:3], v[166:169], v[220:223], v[0:3]
	v_mfma_f32_16x16x32_bf16 v[52:55], v[150:153], v[184:187], v[52:55]
	v_mfma_f32_16x16x32_bf16 v[48:51], v[176:179], v[184:187], v[48:51]
	v_mfma_f32_16x16x32_bf16 v[36:39], v[150:153], v[192:195], v[36:39]
	v_mfma_f32_16x16x32_bf16 v[32:35], v[176:179], v[192:195], v[32:35]
	v_mfma_f32_16x16x32_bf16 v[20:23], v[150:153], v[216:219], v[20:23]
	v_mfma_f32_16x16x32_bf16 v[16:19], v[176:179], v[216:219], v[16:19]
	v_mfma_f32_16x16x32_bf16 v[4:7], v[150:153], v[224:227], v[4:7]
	v_mfma_f32_16x16x32_bf16 v[0:3], v[176:179], v[224:227], v[0:3]
	s_setprio 0
	s_barrier
	s_add_i32 s61, s61, 2
	s_add_u32 s0, s0, 0x100
	s_addc_u32 s1, s1, 0
	s_add_u32 s59, s59, 0x100
	s_addc_u32 s60, s60, 0
	s_cmp_gt_u32 s61, 13
	s_cbranch_scc0 .LBB0_814
	s_and_b64 vcc, exec, s[20:21]
	s_cbranch_vccz .LBB0_817
	s_barrier
